# P1 column tiles interleaved across XCD classes (every workgroup gets 2 gate tiles + 3 QKV tiles instead of 4+1 / 0+5); setprio-free GEMM loops
# speedup vs baseline: 1.0003x; 1.0003x over previous
.LBB0_105:
	s_nop 0
	v_mov_b32_e32 v2, v0
	s_cmpk_gt_i32 s33, 0x27f
	v_readfirstlane_b32 s0, v2
	s_cbranch_scc1 .LBB0_133
	v_bfe_i32 v4, v2, 27, 1
	v_lshlrev_b32_e32 v3, 4, v2
	v_lshrrev_b32_e32 v4, 22, v4
	v_add_u32_e32 v4, v3, v4
	v_and_b32_e32 v4, 0xfffffc00, v4
	v_sub_u32_e32 v4, v3, v4
	v_ashrrev_i32_e32 v1, 31, v2
	v_lshrrev_b32_e32 v5, 4, v4
	v_lshrrev_b32_e32 v1, 26, v1
	v_bitop3_b32 v5, v5, v4, 32 bitop3:0x6c
	v_ashrrev_i32_e32 v4, 31, v4
	v_add_u32_e32 v1, v2, v1
	v_lshrrev_b32_e32 v4, 26, v4
	v_ashrrev_i32_e32 v1, 6, v1
	v_add_u32_e32 v4, v5, v4
	v_lshlrev_b32_e32 v6, 3, v1
	v_ashrrev_i32_e32 v4, 6, v4
	v_and_b32_e32 v6, -16, v6
	v_mul_i32_i24_e32 v7, 64, v4
	v_add_u32_e32 v6, v4, v6
	v_sub_u32_e32 v5, v5, v7
	v_mov_b32_e32 v7, 1
	v_lshlrev_b32_e32 v1, 5, v1
	v_ashrrev_i16_sdwa v5, v7, sext(v5) dst_sel:DWORD dst_unused:UNUSED_PAD src0_sel:DWORD src1_sel:BYTE_0
	v_lshlrev_b32_e32 v8, 1, v6
	v_lshrrev_b32_e32 v9, 2, v6
	v_and_b32_e32 v4, 3, v4
	s_mov_b32 s2, 0xfffe0
	v_and_b32_e32 v1, 32, v1
	v_bfe_i32 v5, v5, 0, 16
	v_and_b32_e32 v8, 24, v8
	v_and_b32_e32 v9, 4, v9
	v_and_or_b32 v4, v6, s2, v4
	v_or3_b32 v4, v4, v9, v8
	v_add_lshl_u32 v5, v1, v5, 1
	v_lshl_add_u32 v191, v4, 12, v5
	v_add_u32_e32 v4, 0x2000, v3
	v_lshl_add_u32 v1, v6, 12, v5
	v_ashrrev_i32_e32 v5, 31, v4
	v_lshrrev_b32_e32 v5, 22, v5
	v_add_u32_e32 v5, v4, v5
	v_ashrrev_i32_e32 v5, 10, v5
	v_mul_i32_i24_e32 v6, 0x400, v5
	v_readlane_b32 s8, v255, 1
	v_sub_u32_e32 v4, v4, v6
	v_readlane_b32 s10, v255, 3
	v_lshrrev_b32_e32 v6, 4, v4
	v_readlane_b32 s11, v255, 4
	s_add_u32 s40, s10, 0x7b00000
	v_bitop3_b32 v4, v6, v4, 32 bitop3:0x6c
	s_addc_u32 s3, s11, 0
	v_ashrrev_i32_e32 v8, 31, v4
	s_add_u32 s44, s10, 0x5300000
	v_lshrrev_b32_e32 v8, 26, v8
	s_addc_u32 s5, s11, 0
	s_lshl_b32 s66, s4, 4
	v_lshlrev_b32_e32 v6, 3, v5
	v_add_u32_e32 v8, v4, v8
	s_lshr_b32 s4, s33, 30
	v_and_b32_e32 v6, -16, v6
	v_ashrrev_i32_e32 v9, 6, v8
	s_add_i32 s4, s33, s4
	s_ashr_i32 s1, s0, 6
	v_add_u32_e32 v6, v9, v6
	v_and_b32_e32 v9, 3, v9
	s_and_b32 s45, s5, 0xffff
	s_ashr_i32 s5, s4, 2
	s_and_b32 s4, s4, -4
	v_and_or_b32 v9, v6, s2, v9
	s_ashr_i32 s2, s0, 8
	s_and_b32 s41, s3, 0xffff
	s_lshl_b32 s3, s1, 10
	s_sub_i32 s4, s33, s4
	s_cmp_lt_i32 s4, 0
	s_movk_i32 s6, 0xa1
	s_cselect_b32 s6, s6, 0xa0
	s_mul_i32 s4, s4, s6
	s_add_i32 s4, s4, s5
	s_mul_hi_i32 s5, s4, 0x66666667
	s_lshr_b32 s6, s5, 31
	s_ashr_i32 s5, s5, 7
	s_add_i32 s5, s5, s6
	s_lshl_b32 s6, s5, 3
	s_mulk_i32 s5, 0x140
	s_sub_i32 s4, s4, s5
	v_and_b32_e32 v8, 0xc0, v8
	s_bfe_u32 s5, s4, 0x3001c
	v_sub_u32_e32 v4, v4, v8
	s_add_i32 s5, s4, s5
	v_lshlrev_b32_e32 v5, 5, v5
	v_ashrrev_i16_sdwa v4, v7, sext(v4) dst_sel:DWORD dst_unused:UNUSED_PAD src0_sel:DWORD src1_sel:BYTE_0
	v_lshlrev_b32_e32 v7, 1, v6
	v_lshrrev_b32_e32 v8, 2, v6
	s_sext_i32_i16 s7, s5
	s_add_i32 s68, s3, 0
	v_and_b32_e32 v5, 32, v5
	v_bfe_i32 v4, v4, 0, 16
	v_and_b32_e32 v7, 24, v7
	v_and_b32_e32 v8, 4, v8
	s_mov_b32 s43, 0x20000
	s_brev_b32 s42, -2
	s_ashr_i32 s61, s7, 3
	s_add_i32 s98, s61, 12
	s_lshr_b32 s98, s98, 5
	s_mul_i32 s99, s98, 20
	s_sub_i32 s61, s61, s99
	s_lshl_b32 s61, s61, 1
	s_add_i32 s61, s61, s98
	s_add_i32 s69, s68, 0x10000
	v_or3_b32 v7, v9, v8, v7
	v_add_lshl_u32 v4, v5, v4, 1
	s_mov_b32 s46, s42
	s_mov_b32 s47, s43
	s_and_b32 s5, s5, 0xfff8
	s_lshl_b32 s65, s61, 20
	s_mov_b32 m0, s69
	s_add_i32 s70, s68, 0x12000
	v_lshl_add_u32 v217, v7, 12, v4
	s_sub_i32 s4, s4, s5
	buffer_load_dwordx4 v191, s[44:47], s65 offen lds
	s_mov_b32 m0, s70
	s_add_i32 s71, s68, 0x14000
	s_add_i32 s6, s6, s66
	s_sext_i32_i16 s4, s4
	buffer_load_dwordx4 v217, s[44:47], s65 offen lds
	s_or_b32 s3, s65, 0x80000
	s_mov_b32 m0, s71
	s_add_i32 s72, s68, 0x16000
	s_add_i32 s60, s6, s4
	buffer_load_dwordx4 v191, s[44:47], s3 offen lds
	s_mov_b32 m0, s72
	s_lshl_b32 s64, s60, 20
	buffer_load_dwordx4 v217, s[44:47], s3 offen lds
	s_mov_b32 m0, s68
	s_add_i32 s73, s68, 0x2000
	v_lshl_add_u32 v216, v6, 12, v4
	buffer_load_dwordx4 v1, s[40:43], s64 offen lds
	s_mov_b32 m0, s73
	s_add_i32 s74, s68, 0x4000
	buffer_load_dwordx4 v216, s[40:43], s64 offen lds
	s_or_b32 s3, s64, 0x80000
	s_mov_b32 m0, s74
	s_add_i32 s75, s68, 0x6000
	buffer_load_dwordx4 v1, s[40:43], s3 offen lds
	s_mov_b32 m0, s75
	s_cmp_eq_u32 s2, 1
	buffer_load_dwordx4 v216, s[40:43], s3 offen lds
	s_cselect_b64 s[50:51], -1, 0
	s_cmp_lg_u32 s2, 1
	s_mov_b32 s53, 0
	v_readlane_b32 s9, v255, 2
	v_readlane_b32 s12, v255, 5
	v_readlane_b32 s13, v255, 6
	v_readlane_b32 s14, v255, 7
	v_readlane_b32 s15, v255, 8
	s_cbranch_scc1 .LBB0_108
	s_barrier

.LBB0_111:
	s_add_i32 s52, s52, 1
	s_lshl_b64 s[38:39], s[52:53], 7
	s_add_u32 s46, s38, s33
	s_addc_u32 s47, s39, s95
	v_cmp_gt_i64_e32 vcc, s[46:47], v[206:207]
	v_cmp_lt_i64_e64 s[38:39], s[46:47], v[204:205]
	s_cbranch_vccnz .LBB0_113
	s_ashr_i32 s47, s46, 31
	s_lshr_b32 s47, s47, 30
	s_add_i32 s47, s46, s47
	s_ashr_i32 s62, s47, 2
	s_and_b32 s47, s47, -4
	s_sub_i32 s46, s46, s47
	s_cmp_lt_i32 s46, 0
	s_movk_i32 s0, 0xa1
	s_cselect_b32 s47, s0, 0xa0
	s_mul_i32 s46, s46, s47
	s_add_i32 s46, s46, s62
	s_mul_hi_i32 s47, s46, 0x66666667
	s_lshr_b32 s62, s47, 31
	s_ashr_i32 s47, s47, 7
	s_add_i32 s47, s47, s62
	s_lshl_b32 s62, s47, 3
	s_mulk_i32 s47, 0x140
	s_sub_i32 s46, s46, s47
	s_bfe_u32 s47, s46, 0x3001c
	s_add_i32 s47, s46, s47
	s_sext_i32_i16 s63, s47
	s_and_b32 s47, s47, 0xfff8
	s_sub_i32 s46, s46, s47
	s_add_i32 s62, s62, s66
	s_sext_i32_i16 s46, s46
	s_add_i32 s97, s62, s46
	s_ashr_i32 s96, s63, 3
	s_add_i32 s98, s96, 12
	s_lshr_b32 s98, s98, 5
	s_mul_i32 s99, s98, 20
	s_sub_i32 s96, s96, s99
	s_lshl_b32 s96, s96, 1
	s_add_i32 s96, s96, s98

	.amdhsa_kernel _Z10hybrid_fwd4Args
		.amdhsa_group_segment_fixed_size 0
		.amdhsa_private_segment_fixed_size 0
		.amdhsa_kernarg_size 128
		.amdhsa_user_sgpr_count 2
		.amdhsa_user_sgpr_dispatch_ptr 0
		.amdhsa_user_sgpr_queue_ptr 0
		.amdhsa_user_sgpr_kernarg_segment_ptr 1
		.amdhsa_user_sgpr_dispatch_id 0
		.amdhsa_user_sgpr_kernarg_preload_length 0
		.amdhsa_user_sgpr_kernarg_preload_offset 0
		.amdhsa_user_sgpr_private_segment_size 0
		.amdhsa_uses_dynamic_stack 0
		.amdhsa_enable_private_segment 0
		.amdhsa_system_sgpr_workgroup_id_x 1
		.amdhsa_system_sgpr_workgroup_id_y 0
		.amdhsa_system_sgpr_workgroup_id_z 0
		.amdhsa_system_sgpr_workgroup_info 0
		.amdhsa_system_vgpr_workitem_id 0
		.amdhsa_next_free_vgpr 256
		.amdhsa_next_free_sgpr 100
		.amdhsa_accum_offset 256
		.amdhsa_reserve_vcc 1
		.amdhsa_float_round_mode_32 0
		.amdhsa_float_round_mode_16_64 0
		.amdhsa_float_denorm_mode_32 3
		.amdhsa_float_denorm_mode_16_64 3
		.amdhsa_dx10_clamp 1
		.amdhsa_ieee_mode 1
		.amdhsa_fp16_overflow 0
		.amdhsa_tg_split 0
		.amdhsa_exception_fp_ieee_invalid_op 0
		.amdhsa_exception_fp_denorm_src 0
		.amdhsa_exception_fp_ieee_div_zero 0
		.amdhsa_exception_fp_ieee_overflow 0
		.amdhsa_exception_fp_ieee_underflow 0
		.amdhsa_exception_fp_ieee_inexact 0
		.amdhsa_exception_int_div_zero 0
	.end_amdhsa_kernel

amdhsa.kernels:
  - .agpr_count:     0
    .args:
      - .offset:         0
        .size:           128
        .value_kind:     by_value
    .group_segment_fixed_size: 0
    .kernarg_segment_align: 8
    .kernarg_segment_size: 128
    .language:       OpenCL C
    .language_version:
      - 2
      - 0
    .max_flat_workgroup_size: 512
    .name:           _Z10hybrid_fwd4Args
    .private_segment_fixed_size: 0
    .sgpr_count:     106
    .sgpr_spill_count: 77
    .symbol:         _Z10hybrid_fwd4Args.kd
    .uniform_work_group_size: 1
    .uses_dynamic_stack: false
    .vgpr_count:     256
    .vgpr_spill_count: 0
    .wavefront_size: 64
